# P2 QK^T LDS reads pipelined 2 groups ahead; P8 first half-trip peeled with C=0 MFMAs (no accumulator zeroing); conv waits vmcnt(40)
# speedup vs baseline: 1.0002x; 1.0002x over previous
.LBB0_247:
	s_cmp_lt_u32 s99, 2
	s_cbranch_scc1 .Lcv_slow_vc
	s_cmp_eq_u32 s99, 3
	s_cbranch_scc1 .Lcv_f40_vc
	s_waitcnt vmcnt(32)
	s_branch .Lcv_cont_vc
.Lcv_slow_vc:
	s_waitcnt vmcnt(0)
	s_branch .Lcv_cont_vc
.Lcv_f40_vc:
	s_waitcnt vmcnt(40)
.Lcv_cont_vc:
	s_cmp_eq_u32 s99, 2
	s_cselect_b32 s99, 3, s99
	v_mul_f32_e32 v196, s33, v128
	v_mul_f32_e32 v214, s33, v132
	v_mov_b32_e32 v217, v197
	v_cvt_pk_fp8_f32 v217, v196, v214
	v_mul_f32_e32 v196, s33, v129
	v_mul_f32_e32 v214, s33, v133
	v_mov_b32_e32 v218, v197
	v_cvt_pk_fp8_f32 v218, v196, v214
	v_mul_f32_e32 v196, s33, v137
	v_mul_f32_e32 v214, s33, v141
	v_mov_b32_e32 v219, v197
	v_cvt_pk_fp8_f32 v218, v196, v214 op_sel:[0,0,1]
	v_mul_f32_e32 v196, s33, v130
	v_mul_f32_e32 v214, s33, v134
	v_cvt_pk_fp8_f32 v219, v196, v214
	v_mul_f32_e32 v196, s33, v131
	v_mul_f32_e32 v214, s33, v135
	v_mov_b32_e32 v220, v197
	v_cvt_pk_fp8_f32 v220, v196, v214
	v_mul_f32_e32 v196, s33, v139
	v_mul_f32_e32 v214, s33, v143
	v_mov_b32_e32 v221, v197
	v_cvt_pk_fp8_f32 v220, v196, v214 op_sel:[0,0,1]
	v_mul_f32_e32 v196, s33, v144
	v_mul_f32_e32 v214, s33, v148
	v_cvt_pk_fp8_f32 v221, v196, v214
	v_mul_f32_e32 v196, s33, v145
	v_mul_f32_e32 v214, s33, v149
	v_mov_b32_e32 v222, v197
	v_cvt_pk_fp8_f32 v222, v196, v214
	v_mul_f32_e32 v196, s33, v153
	v_mul_f32_e32 v214, s33, v157
	v_mul_f32_e32 v215, s33, v136
	v_mul_f32_e32 v216, s33, v140
	v_cvt_pk_fp8_f32 v222, v196, v214 op_sel:[0,0,1]
	v_mul_f32_e32 v196, s33, v146
	v_mul_f32_e32 v214, s33, v150
	v_mov_b32_e32 v223, v197
	v_cvt_pk_fp8_f32 v217, v215, v216 op_sel:[0,0,1]
	v_mul_f32_e32 v215, s33, v138
	v_mul_f32_e32 v216, s33, v142
	v_cvt_pk_fp8_f32 v223, v196, v214
	v_mul_f32_e32 v196, s33, v147
	v_mul_f32_e32 v214, s33, v151
	v_mov_b32_e32 v224, v197
	v_cvt_pk_fp8_f32 v219, v215, v216 op_sel:[0,0,1]
	v_mul_f32_e32 v215, s33, v152
	v_mul_f32_e32 v216, s33, v156
	v_cvt_pk_fp8_f32 v224, v196, v214
	v_cvt_pk_fp8_f32 v221, v215, v216 op_sel:[0,0,1]
	v_mul_f32_e32 v215, s33, v154
	v_mul_f32_e32 v216, s33, v158
	v_cvt_pk_fp8_f32 v223, v215, v216 op_sel:[0,0,1]
	v_mul_f32_e32 v196, s33, v155
	v_mul_f32_e32 v214, s33, v159
	v_cvt_pk_fp8_f32 v224, v196, v214 op_sel:[0,0,1]
	ds_write2_b32 v193, v217, v221 offset1:8
	ds_write2_b32 v193, v218, v222 offset0:33 offset1:41
	ds_write2_b32 v193, v219, v223 offset0:66 offset1:74
	ds_write2_b32 v193, v220, v224 offset0:99 offset1:107
	v_mul_f32_e32 v196, s33, v160
	v_mul_f32_e32 v214, s33, v164
	v_mov_b32_e32 v217, v197
	v_cvt_pk_fp8_f32 v217, v196, v214
	v_mul_f32_e32 v196, s33, v161
	v_mul_f32_e32 v214, s33, v165
	v_mov_b32_e32 v218, v197
	v_cvt_pk_fp8_f32 v218, v196, v214
	v_mul_f32_e32 v196, s33, v169
	v_mul_f32_e32 v214, s33, v173
	v_mov_b32_e32 v219, v197
	v_cvt_pk_fp8_f32 v218, v196, v214 op_sel:[0,0,1]
	v_mul_f32_e32 v196, s33, v162
	v_mul_f32_e32 v214, s33, v166
	v_cvt_pk_fp8_f32 v219, v196, v214
	v_mul_f32_e32 v196, s33, v163
	v_mul_f32_e32 v214, s33, v167
	v_mov_b32_e32 v220, v197
	v_cvt_pk_fp8_f32 v220, v196, v214
	v_mul_f32_e32 v196, s33, v171
	v_mul_f32_e32 v214, s33, v175
	v_mov_b32_e32 v221, v197
	v_cvt_pk_fp8_f32 v220, v196, v214 op_sel:[0,0,1]
	v_mul_f32_e32 v196, s33, v176
	v_mul_f32_e32 v214, s33, v180
	v_cvt_pk_fp8_f32 v221, v196, v214
	v_mul_f32_e32 v196, s33, v177
	v_mul_f32_e32 v214, s33, v181
	v_mov_b32_e32 v222, v197
	v_cvt_pk_fp8_f32 v222, v196, v214
	v_mul_f32_e32 v196, s33, v185
	v_mul_f32_e32 v214, s33, v189
	v_mul_f32_e32 v215, s33, v168
	v_mul_f32_e32 v216, s33, v172
	v_cvt_pk_fp8_f32 v222, v196, v214 op_sel:[0,0,1]
	v_mul_f32_e32 v196, s33, v178
	v_mul_f32_e32 v214, s33, v182
	v_mov_b32_e32 v223, v197
	v_cvt_pk_fp8_f32 v217, v215, v216 op_sel:[0,0,1]
	v_mul_f32_e32 v215, s33, v170
	v_mul_f32_e32 v216, s33, v174
	v_cvt_pk_fp8_f32 v223, v196, v214
	v_mul_f32_e32 v196, s33, v179
	v_mul_f32_e32 v214, s33, v183
	v_mov_b32_e32 v224, v197
	v_cvt_pk_fp8_f32 v219, v215, v216 op_sel:[0,0,1]
	v_mul_f32_e32 v215, s33, v184
	v_mul_f32_e32 v216, s33, v188
	v_cvt_pk_fp8_f32 v224, v196, v214
	v_cvt_pk_fp8_f32 v221, v215, v216 op_sel:[0,0,1]
	v_mul_f32_e32 v215, s33, v186
	v_mul_f32_e32 v216, s33, v190
	v_cvt_pk_fp8_f32 v223, v215, v216 op_sel:[0,0,1]
	v_mul_f32_e32 v196, s33, v187
	v_mul_f32_e32 v214, s33, v191
	v_cvt_pk_fp8_f32 v224, v196, v214 op_sel:[0,0,1]
	ds_write2_b32 v193, v217, v221 offset0:16 offset1:24
	ds_write2_b32 v193, v218, v222 offset0:49 offset1:57
	ds_write2_b32 v193, v219, v223 offset0:82 offset1:90
	ds_write2_b32 v193, v220, v224 offset0:115 offset1:123
	s_waitcnt lgkmcnt(0)
	ds_read2_b32 v[214:215], v195 offset1:1
	ds_read2_b32 v[216:217], v195 offset0:2 offset1:3
	ds_read2_b32 v[218:219], v208 offset1:1
	ds_read2_b32 v[220:221], v209 offset1:1
	v_lshl_add_u64 v[222:223], s[8:9], 0, v[200:201]
	v_lshl_add_u64 v[208:209], v[222:223], 0, v[198:199]
	s_addk_i32 s28, 0xba0
	s_waitcnt lgkmcnt(2)
	global_store_dwordx4 v[208:209], v[214:217], off nt
	v_lshl_add_u64 v[208:209], s[8:9], 0, v[202:203]
	v_lshl_add_u64 v[208:209], v[208:209], 0, v[198:199]
	s_waitcnt lgkmcnt(0)
	global_store_dwordx4 v[208:209], v[218:221], off nt
	ds_read2_b32 v[208:209], v210 offset1:1
	ds_read2_b32 v[210:211], v211 offset1:1
	ds_read2_b32 v[214:215], v212 offset1:1
	ds_read2_b32 v[216:217], v213 offset1:1
	v_lshl_add_u64 v[218:219], s[8:9], 0, v[204:205]
	v_lshl_add_u64 v[212:213], v[218:219], 0, v[198:199]
	s_add_i32 s29, s29, 0x17400
	s_waitcnt lgkmcnt(2)
	global_store_dwordx4 v[212:213], v[208:211], off nt
	s_add_i32 s30, s30, 0x2e800
	s_addk_i32 s31, 0x1740
	v_lshl_add_u64 v[208:209], s[8:9], 0, v[206:207]
	v_lshl_add_u64 v[208:209], v[208:209], 0, v[198:199]
	s_waitcnt lgkmcnt(0)
	global_store_dwordx4 v[208:209], v[214:217], off nt
	s_waitcnt lgkmcnt(0)
	s_cmp_gt_i32 s34, 0x1745f
	s_cselect_b64 s[12:13], -1, 0

.Lcv_cont_va:
	v_mul_f32_e32 v196, s16, v0
	v_mul_f32_e32 v208, s16, v4
	v_mov_b32_e32 v211, v197
	v_cvt_pk_fp8_f32 v211, v196, v208
	v_mul_f32_e32 v196, s16, v1
	v_mul_f32_e32 v208, s16, v5
	v_mov_b32_e32 v212, v197
	v_cvt_pk_fp8_f32 v212, v196, v208
	v_mul_f32_e32 v196, s16, v9
	v_mul_f32_e32 v208, s16, v13
	v_mov_b32_e32 v213, v197
	v_cvt_pk_fp8_f32 v212, v196, v208 op_sel:[0,0,1]
	v_mul_f32_e32 v196, s16, v2
	v_mul_f32_e32 v208, s16, v6
	v_cvt_pk_fp8_f32 v213, v196, v208
	v_mul_f32_e32 v196, s16, v3
	v_mul_f32_e32 v208, s16, v7
	v_mov_b32_e32 v214, v197
	v_cvt_pk_fp8_f32 v214, v196, v208
	v_mul_f32_e32 v196, s16, v11
	v_mul_f32_e32 v208, s16, v15
	v_mov_b32_e32 v215, v197
	v_cvt_pk_fp8_f32 v214, v196, v208 op_sel:[0,0,1]
	v_mul_f32_e32 v196, s16, v16
	v_mul_f32_e32 v208, s16, v20
	v_cvt_pk_fp8_f32 v215, v196, v208
	v_mul_f32_e32 v196, s16, v17
	v_mul_f32_e32 v208, s16, v21
	v_mov_b32_e32 v216, v197
	v_cvt_pk_fp8_f32 v216, v196, v208
	v_mul_f32_e32 v196, s16, v25
	v_mul_f32_e32 v208, s16, v29
	v_mul_f32_e32 v209, s16, v8
	v_mul_f32_e32 v210, s16, v12
	v_cvt_pk_fp8_f32 v216, v196, v208 op_sel:[0,0,1]
	v_mul_f32_e32 v196, s16, v18
	v_mul_f32_e32 v208, s16, v22
	v_mov_b32_e32 v217, v197
	v_cvt_pk_fp8_f32 v211, v209, v210 op_sel:[0,0,1]
	v_mul_f32_e32 v209, s16, v10
	v_mul_f32_e32 v210, s16, v14
	v_cvt_pk_fp8_f32 v217, v196, v208
	v_mul_f32_e32 v196, s16, v19
	v_mul_f32_e32 v208, s16, v23
	v_mov_b32_e32 v218, v197
	v_cvt_pk_fp8_f32 v213, v209, v210 op_sel:[0,0,1]
	v_mul_f32_e32 v209, s16, v24
	v_mul_f32_e32 v210, s16, v28
	v_cvt_pk_fp8_f32 v218, v196, v208
	v_cvt_pk_fp8_f32 v215, v209, v210 op_sel:[0,0,1]
	v_mul_f32_e32 v209, s16, v26
	v_mul_f32_e32 v210, s16, v30
	v_cvt_pk_fp8_f32 v217, v209, v210 op_sel:[0,0,1]
	v_mul_f32_e32 v196, s16, v27
	v_mul_f32_e32 v208, s16, v31
	v_cvt_pk_fp8_f32 v218, v196, v208 op_sel:[0,0,1]
	ds_write2_b32 v193, v211, v215 offset1:8
	ds_write2_b32 v193, v212, v216 offset0:33 offset1:41
	ds_write2_b32 v193, v213, v217 offset0:66 offset1:74
	ds_write2_b32 v193, v214, v218 offset0:99 offset1:107
	v_mul_f32_e32 v196, s16, v32
	v_mul_f32_e32 v208, s16, v36
	v_mov_b32_e32 v211, v197
	v_cvt_pk_fp8_f32 v211, v196, v208
	v_mul_f32_e32 v196, s16, v33
	v_mul_f32_e32 v208, s16, v37
	v_mov_b32_e32 v212, v197
	v_cvt_pk_fp8_f32 v212, v196, v208
	v_mul_f32_e32 v196, s16, v49
	v_mul_f32_e32 v208, s16, v61
	v_mov_b32_e32 v213, v197
	v_cvt_pk_fp8_f32 v212, v196, v208 op_sel:[0,0,1]
	v_mul_f32_e32 v196, s16, v34
	v_mul_f32_e32 v208, s16, v38
	v_cvt_pk_fp8_f32 v213, v196, v208
	v_mul_f32_e32 v196, s16, v35
	v_mul_f32_e32 v208, s16, v39
	v_mov_b32_e32 v214, v197
	v_cvt_pk_fp8_f32 v214, v196, v208
	v_mul_f32_e32 v196, s16, v51
	v_mul_f32_e32 v208, s16, v63
	v_mov_b32_e32 v215, v197
	v_cvt_pk_fp8_f32 v214, v196, v208 op_sel:[0,0,1]
	v_mul_f32_e32 v196, s16, v40
	v_mul_f32_e32 v208, s16, v44
	v_cvt_pk_fp8_f32 v215, v196, v208
	v_mul_f32_e32 v196, s16, v41
	v_mul_f32_e32 v208, s16, v45
	v_mov_b32_e32 v216, v197
	v_cvt_pk_fp8_f32 v216, v196, v208
	v_mul_f32_e32 v196, s16, v53
	v_mul_f32_e32 v208, s16, v57
	v_mul_f32_e32 v209, s16, v48
	v_mul_f32_e32 v210, s16, v60
	v_cvt_pk_fp8_f32 v216, v196, v208 op_sel:[0,0,1]
	v_mul_f32_e32 v196, s16, v42
	v_mul_f32_e32 v208, s16, v46
	v_mov_b32_e32 v217, v197
	v_cvt_pk_fp8_f32 v211, v209, v210 op_sel:[0,0,1]
	v_mul_f32_e32 v209, s16, v50
	v_mul_f32_e32 v210, s16, v62
	v_cvt_pk_fp8_f32 v217, v196, v208
	v_mul_f32_e32 v196, s16, v43
	v_mul_f32_e32 v208, s16, v47
	v_mov_b32_e32 v218, v197
	v_cvt_pk_fp8_f32 v213, v209, v210 op_sel:[0,0,1]
	v_mul_f32_e32 v209, s16, v52
	v_mul_f32_e32 v210, s16, v56
	v_cvt_pk_fp8_f32 v218, v196, v208
	v_cvt_pk_fp8_f32 v215, v209, v210 op_sel:[0,0,1]
	v_mul_f32_e32 v209, s16, v54
	v_mul_f32_e32 v210, s16, v58
	v_cvt_pk_fp8_f32 v217, v209, v210 op_sel:[0,0,1]
	v_mul_f32_e32 v196, s16, v55
	v_mul_f32_e32 v208, s16, v59
	v_cvt_pk_fp8_f32 v218, v196, v208 op_sel:[0,0,1]
	ds_write2_b32 v193, v211, v215 offset0:16 offset1:24
	ds_write2_b32 v193, v212, v216 offset0:49 offset1:57
	ds_write2_b32 v193, v213, v217 offset0:82 offset1:90
	ds_write2_b32 v193, v214, v218 offset0:115 offset1:123
	s_waitcnt lgkmcnt(0)
	ds_read2_b32 v[210:211], v195 offset1:1
	ds_read2_b32 v[212:213], v195 offset0:2 offset1:3
	v_add_u32_e32 v208, 0x420, v195
	v_add_u32_e32 v209, 0x428, v195
	ds_read2_b32 v[214:215], v208 offset1:1
	ds_read2_b32 v[216:217], v209 offset1:1
	v_lshl_add_u64 v[218:219], s[0:1], 0, v[200:201]
	v_lshl_add_u64 v[218:219], v[218:219], 0, v[198:199]
	s_waitcnt lgkmcnt(2)
	global_store_dwordx4 v[218:219], v[210:213], off nt
	v_lshl_add_u64 v[222:223], s[0:1], 0, v[204:205]
	v_lshl_add_u64 v[222:223], v[222:223], 0, v[198:199]
	v_lshl_add_u64 v[210:211], s[0:1], 0, v[202:203]
	v_lshl_add_u64 v[210:211], v[210:211], 0, v[198:199]
	s_waitcnt lgkmcnt(0)
	global_store_dwordx4 v[210:211], v[214:217], off nt
	v_add_u32_e32 v210, 0x840, v195
	v_add_u32_e32 v211, 0x848, v195
	ds_read2_b32 v[214:215], v210 offset1:1
	ds_read2_b32 v[216:217], v211 offset1:1
	v_add_u32_e32 v212, 0xc60, v195
	v_add_u32_e32 v213, 0xc68, v195
	ds_read2_b32 v[218:219], v212 offset1:1
	ds_read2_b32 v[220:221], v213 offset1:1
	s_cmp_gt_i32 s34, 0x17c1f
	s_waitcnt lgkmcnt(2)
	global_store_dwordx4 v[222:223], v[214:217], off nt
	s_mov_b64 s[12:13], -1
	s_nop 0
	v_lshl_add_u64 v[214:215], s[0:1], 0, v[206:207]
	v_lshl_add_u64 v[214:215], v[214:215], 0, v[198:199]
	s_waitcnt lgkmcnt(0)
	global_store_dwordx4 v[214:215], v[218:221], off nt
	s_waitcnt lgkmcnt(0)
	s_cbranch_scc1 .LBB0_248
	s_cmp_gt_i32 s34, 0x1745f
	s_cbranch_scc1 .Lcv_skip_a
	s_cmp_gt_i32 s34, 0xf45f
	s_mov_b64 s[14:15], -1
	s_cbranch_scc0 .LBB0_260
	s_add_i32 s0, s28, 0xfffefc20
	s_lshr_b32 s6, s0, 10
	s_add_i32 s0, s29, 0x1f000
	s_and_b32 s14, s0, 0x7e0
	s_add_i32 s0, s31, 0x1f00
	s_and_b32 s15, s0, 0x780
	s_lshl_b64 s[0:1], s[6:7], 22
	s_lshl_b64 s[12:13], s[6:7], 24
	v_readlane_b32 s36, v251, 2
	v_readlane_b32 s37, v251, 3
	s_add_u32 s6, s36, s12
	s_addc_u32 s12, s37, s13
	s_lshl_b32 s13, s15, 13
	s_add_u32 s6, s6, s13
	s_addc_u32 s13, s12, 0
	s_lshl_b32 s12, s14, 2
	s_add_u32 s12, s6, s12
	s_addc_u32 s13, s13, 0
	s_add_u32 s0, s18, s0
	s_addc_u32 s1, s19, s1
	s_lshl_b32 s6, s14, 11
	s_add_u32 s0, s0, s6
	s_addc_u32 s1, s1, 0
	s_add_u32 s0, s0, s15
	v_readlane_b32 s38, v251, 4
	v_readlane_b32 s39, v251, 5
	v_readlane_b32 s40, v251, 6
	v_readlane_b32 s41, v251, 7
	v_readlane_b32 s42, v251, 8
	v_readlane_b32 s43, v251, 9
	s_addc_u32 s1, s1, 0
	s_mov_b64 s[14:15], 0

.Lcv_cont_vb:
	v_mul_f32_e32 v196, s17, v64
	v_mul_f32_e32 v214, s17, v68
	v_mov_b32_e32 v217, v197
	v_cvt_pk_fp8_f32 v217, v196, v214
	v_mul_f32_e32 v196, s17, v65
	v_mul_f32_e32 v214, s17, v69
	v_mov_b32_e32 v218, v197
	v_cvt_pk_fp8_f32 v218, v196, v214
	v_mul_f32_e32 v196, s17, v73
	v_mul_f32_e32 v214, s17, v77
	v_mov_b32_e32 v219, v197
	v_cvt_pk_fp8_f32 v218, v196, v214 op_sel:[0,0,1]
	v_mul_f32_e32 v196, s17, v66
	v_mul_f32_e32 v214, s17, v70
	v_cvt_pk_fp8_f32 v219, v196, v214
	v_mul_f32_e32 v196, s17, v67
	v_mul_f32_e32 v214, s17, v71
	v_mov_b32_e32 v220, v197
	v_cvt_pk_fp8_f32 v220, v196, v214
	v_mul_f32_e32 v196, s17, v75
	v_mul_f32_e32 v214, s17, v79
	v_mov_b32_e32 v221, v197
	v_cvt_pk_fp8_f32 v220, v196, v214 op_sel:[0,0,1]
	v_mul_f32_e32 v196, s17, v80
	v_mul_f32_e32 v214, s17, v84
	v_cvt_pk_fp8_f32 v221, v196, v214
	v_mul_f32_e32 v196, s17, v81
	v_mul_f32_e32 v214, s17, v85
	v_mov_b32_e32 v222, v197
	v_cvt_pk_fp8_f32 v222, v196, v214
	v_mul_f32_e32 v196, s17, v89
	v_mul_f32_e32 v214, s17, v93
	v_mul_f32_e32 v215, s17, v72
	v_mul_f32_e32 v216, s17, v76
	v_cvt_pk_fp8_f32 v222, v196, v214 op_sel:[0,0,1]
	v_mul_f32_e32 v196, s17, v82
	v_mul_f32_e32 v214, s17, v86
	v_mov_b32_e32 v223, v197
	v_cvt_pk_fp8_f32 v217, v215, v216 op_sel:[0,0,1]
	v_mul_f32_e32 v215, s17, v74
	v_mul_f32_e32 v216, s17, v78
	v_cvt_pk_fp8_f32 v223, v196, v214
	v_mul_f32_e32 v196, s17, v83
	v_mul_f32_e32 v214, s17, v87
	v_mov_b32_e32 v224, v197
	v_cvt_pk_fp8_f32 v219, v215, v216 op_sel:[0,0,1]
	v_mul_f32_e32 v215, s17, v88
	v_mul_f32_e32 v216, s17, v92
	v_cvt_pk_fp8_f32 v224, v196, v214
	v_cvt_pk_fp8_f32 v221, v215, v216 op_sel:[0,0,1]
	v_mul_f32_e32 v215, s17, v90
	v_mul_f32_e32 v216, s17, v94
	v_cvt_pk_fp8_f32 v223, v215, v216 op_sel:[0,0,1]
	v_mul_f32_e32 v196, s17, v91
	v_mul_f32_e32 v214, s17, v95
	v_cvt_pk_fp8_f32 v224, v196, v214 op_sel:[0,0,1]
	ds_write2_b32 v193, v217, v221 offset1:8
	ds_write2_b32 v193, v218, v222 offset0:33 offset1:41
	ds_write2_b32 v193, v219, v223 offset0:66 offset1:74
	ds_write2_b32 v193, v220, v224 offset0:99 offset1:107
	v_mul_f32_e32 v196, s17, v96
	v_mul_f32_e32 v214, s17, v100
	v_mov_b32_e32 v217, v197
	v_cvt_pk_fp8_f32 v217, v196, v214
	v_mul_f32_e32 v196, s17, v97
	v_mul_f32_e32 v214, s17, v101
	v_mov_b32_e32 v218, v197
	v_cvt_pk_fp8_f32 v218, v196, v214
	v_mul_f32_e32 v196, s17, v105
	v_mul_f32_e32 v214, s17, v109
	v_mov_b32_e32 v219, v197
	v_cvt_pk_fp8_f32 v218, v196, v214 op_sel:[0,0,1]
	v_mul_f32_e32 v196, s17, v98
	v_mul_f32_e32 v214, s17, v102
	v_cvt_pk_fp8_f32 v219, v196, v214
	v_mul_f32_e32 v196, s17, v99
	v_mul_f32_e32 v214, s17, v103
	v_mov_b32_e32 v220, v197
	v_cvt_pk_fp8_f32 v220, v196, v214
	v_mul_f32_e32 v196, s17, v107
	v_mul_f32_e32 v214, s17, v111
	v_mov_b32_e32 v221, v197
	v_cvt_pk_fp8_f32 v220, v196, v214 op_sel:[0,0,1]
	v_mul_f32_e32 v196, s17, v112
	v_mul_f32_e32 v214, s17, v116
	v_cvt_pk_fp8_f32 v221, v196, v214
	v_mul_f32_e32 v196, s17, v113
	v_mul_f32_e32 v214, s17, v117
	v_mov_b32_e32 v222, v197
	v_cvt_pk_fp8_f32 v222, v196, v214
	v_mul_f32_e32 v196, s17, v121
	v_mul_f32_e32 v214, s17, v125
	v_mul_f32_e32 v215, s17, v104
	v_mul_f32_e32 v216, s17, v108
	v_cvt_pk_fp8_f32 v222, v196, v214 op_sel:[0,0,1]
	v_mul_f32_e32 v196, s17, v114
	v_mul_f32_e32 v214, s17, v118
	v_mov_b32_e32 v223, v197
	v_cvt_pk_fp8_f32 v217, v215, v216 op_sel:[0,0,1]
	v_mul_f32_e32 v215, s17, v106
	v_mul_f32_e32 v216, s17, v110
	v_cvt_pk_fp8_f32 v223, v196, v214
	v_mul_f32_e32 v196, s17, v115
	v_mul_f32_e32 v214, s17, v119
	v_mov_b32_e32 v224, v197
	v_cvt_pk_fp8_f32 v219, v215, v216 op_sel:[0,0,1]
	v_mul_f32_e32 v215, s17, v120
	v_mul_f32_e32 v216, s17, v124
	v_cvt_pk_fp8_f32 v224, v196, v214
	v_cvt_pk_fp8_f32 v221, v215, v216 op_sel:[0,0,1]
	v_mul_f32_e32 v215, s17, v122
	v_mul_f32_e32 v216, s17, v126
	v_cvt_pk_fp8_f32 v223, v215, v216 op_sel:[0,0,1]
	v_mul_f32_e32 v196, s17, v123
	v_mul_f32_e32 v214, s17, v127
	v_cvt_pk_fp8_f32 v224, v196, v214 op_sel:[0,0,1]
	ds_write2_b32 v193, v217, v221 offset0:16 offset1:24
	ds_write2_b32 v193, v218, v222 offset0:49 offset1:57
	ds_write2_b32 v193, v219, v223 offset0:82 offset1:90
	ds_write2_b32 v193, v220, v224 offset0:115 offset1:123
	s_waitcnt lgkmcnt(0)
	ds_read2_b32 v[214:215], v195 offset1:1
	ds_read2_b32 v[216:217], v195 offset0:2 offset1:3
	ds_read2_b32 v[218:219], v208 offset1:1
	ds_read2_b32 v[220:221], v209 offset1:1
	v_lshl_add_u64 v[222:223], s[4:5], 0, v[200:201]
	v_lshl_add_u64 v[222:223], v[222:223], 0, v[198:199]
	s_andn2_b64 vcc, exec, s[10:11]
	s_waitcnt lgkmcnt(2)
	global_store_dwordx4 v[222:223], v[214:217], off nt
	v_lshl_add_u64 v[222:223], s[4:5], 0, v[204:205]
	v_lshl_add_u64 v[222:223], v[222:223], 0, v[198:199]
	v_lshl_add_u64 v[214:215], s[4:5], 0, v[202:203]
	v_lshl_add_u64 v[214:215], v[214:215], 0, v[198:199]
	s_waitcnt lgkmcnt(0)
	global_store_dwordx4 v[214:215], v[218:221], off nt
	ds_read2_b32 v[214:215], v210 offset1:1
	ds_read2_b32 v[216:217], v211 offset1:1
	ds_read2_b32 v[218:219], v212 offset1:1
	ds_read2_b32 v[220:221], v213 offset1:1
	s_mov_b64 s[12:13], -1
	s_waitcnt lgkmcnt(2)
	global_store_dwordx4 v[222:223], v[214:217], off nt
	s_nop 1
	v_lshl_add_u64 v[214:215], s[4:5], 0, v[206:207]
	v_lshl_add_u64 v[214:215], v[214:215], 0, v[198:199]
	s_waitcnt lgkmcnt(0)
	global_store_dwordx4 v[214:215], v[218:221], off nt
	s_waitcnt lgkmcnt(0)
	s_cbranch_vccnz .LBB0_248
	s_cmp_gt_i32 s34, 0x1707f
	s_cbranch_scc1 .Lcv_skip_b
	s_cmp_gt_i32 s34, 0xf07f
	s_cbranch_scc0 .LBB0_268
	s_add_i32 s4, s28, 0xffff0000
	s_lshr_b32 s6, s4, 10
	s_add_i32 s4, s29, 0x26c00
	s_and_b32 s12, s4, 0x7e0
	s_add_i32 s4, s31, 0x26c0
	s_and_b32 s13, s4, 0x780
	s_lshl_b64 s[4:5], s[6:7], 22
	s_lshl_b64 s[10:11], s[6:7], 24
	v_readlane_b32 s36, v251, 2
	v_readlane_b32 s37, v251, 3
	s_add_u32 s6, s36, s10
	s_addc_u32 s10, s37, s11
	s_lshl_b32 s11, s13, 13
	s_add_u32 s6, s6, s11
	s_addc_u32 s11, s10, 0
	s_lshl_b32 s10, s12, 2
	s_add_u32 s10, s6, s10
	s_addc_u32 s11, s11, 0
	s_add_u32 s4, s18, s4
	s_addc_u32 s5, s19, s5
	s_lshl_b32 s6, s12, 11
	s_add_u32 s4, s4, s6
	s_addc_u32 s5, s5, 0
	s_add_u32 s4, s4, s13
	v_readlane_b32 s38, v251, 4
	v_readlane_b32 s39, v251, 5
	v_readlane_b32 s40, v251, 6
	v_readlane_b32 s41, v251, 7
	v_readlane_b32 s42, v251, 8
	v_readlane_b32 s43, v251, 9
	s_addc_u32 s5, s5, 0
	s_mov_b64 s[12:13], 0

.LBB0_701:
	v_lshl_add_u32 v56, s5, 7, v79
	v_lshlrev_b64 v[0:1], s4, v[56:57]
	v_lshl_add_u64 v[74:75], v[0:1], 0, s[40:41]
	v_mov_b64_e32 v[0:1], s[46:47]
	v_mad_u64_u32 v[0:1], s[4:5], v74, s30, v[0:1]
	v_mov_b32_e32 v2, v1
	v_mad_u64_u32 v[2:3], s[4:5], v75, s30, v[2:3]
	v_mov_b32_e32 v1, v2
	s_ashr_i32 s3, s2, 31
	v_lshl_add_u64 v[0:1], s[2:3], 1, v[0:1]
	v_lshl_add_u64 v[0:1], v[72:73], 1, v[0:1]
	global_load_dwordx4 v[48:51], v[0:1], off
	global_load_dwordx4 v[44:47], v[0:1], off offset:64
	global_load_dwordx4 v[40:43], v[0:1], off offset:128
	global_load_dwordx4 v[24:27], v[0:1], off offset:192
	s_waitcnt vmcnt(0)
	s_barrier
	ds_read_b128 v[200:203], v136
	ds_read_b128 v[204:207], v137
	ds_read_b128 v[208:211], v138
	ds_read_b128 v[212:215], v139
	ds_read_b128 v[216:219], v140
	ds_read_b128 v[220:223], v141
	ds_read_b128 v[224:227], v142
	ds_read_b128 v[228:231], v143
	v_add_u32_e32 v155, s80, v59
	v_add_u32_e32 v154, s80, v61
	v_add_u32_e32 v153, s80, v63
	v_add_u32_e32 v152, s80, v65
	s_andn2_b64 vcc, exec, s[6:7]
	v_cmp_lt_i32_e64 s[18:19], -1, v155
	v_lshlrev_b32_e32 v56, 1, v54
	v_cmp_lt_i32_e64 s[16:17], -1, v154
	v_lshlrev_b32_e32 v76, 1, v58
	v_cmp_lt_i32_e64 s[14:15], -1, v153
	v_cmp_lt_i32_e64 s[12:13], -1, v152
	v_add_u32_e32 v151, s80, v67
	v_add_u32_e32 v150, s80, v69
	ds_read_b128 v[232:235], v136 offset:8192
	ds_read_b128 v[236:239], v137 offset:8192
	ds_read_b128 v[240:243], v138 offset:8192
	ds_read_b128 v[244:247], v139 offset:8192
	s_waitcnt vmcnt(0)
	s_waitcnt lgkmcnt(8)
	v_mfma_f32_16x16x32_bf16 v[36:39], v[200:203], v[48:51], 0
	v_mfma_f32_16x16x32_bf16 v[36:39], v[204:207], v[44:47], v[36:39]
	v_mfma_f32_16x16x32_bf16 v[36:39], v[208:211], v[40:43], v[36:39]
	v_mfma_f32_16x16x32_bf16 v[36:39], v[212:215], v[24:27], v[36:39]
	ds_read_b128 v[200:203], v140 offset:8192
	ds_read_b128 v[204:207], v141 offset:8192
	ds_read_b128 v[208:211], v142 offset:8192
	ds_read_b128 v[212:215], v143 offset:8192
	s_waitcnt lgkmcnt(8)
	v_mfma_f32_16x16x32_bf16 v[32:35], v[216:219], v[48:51], 0
	v_mfma_f32_16x16x32_bf16 v[32:35], v[220:223], v[44:47], v[32:35]
	v_mfma_f32_16x16x32_bf16 v[32:35], v[224:227], v[40:43], v[32:35]
	v_mfma_f32_16x16x32_bf16 v[32:35], v[228:231], v[24:27], v[32:35]
	ds_read_b128 v[216:219], v136 offset:16384
	ds_read_b128 v[220:223], v137 offset:16384
	ds_read_b128 v[224:227], v138 offset:16384
	ds_read_b128 v[228:231], v139 offset:16384
	s_waitcnt lgkmcnt(8)
	v_mfma_f32_16x16x32_bf16 v[28:31], v[232:235], v[48:51], 0
	v_mfma_f32_16x16x32_bf16 v[28:31], v[236:239], v[44:47], v[28:31]
	v_mfma_f32_16x16x32_bf16 v[28:31], v[240:243], v[40:43], v[28:31]
	v_mfma_f32_16x16x32_bf16 v[28:31], v[244:247], v[24:27], v[28:31]
	ds_read_b128 v[232:235], v140 offset:16384
	ds_read_b128 v[236:239], v141 offset:16384
	ds_read_b128 v[240:243], v142 offset:16384
	ds_read_b128 v[244:247], v143 offset:16384
	s_waitcnt lgkmcnt(8)
	v_mfma_f32_16x16x32_bf16 v[20:23], v[200:203], v[48:51], 0
	v_mfma_f32_16x16x32_bf16 v[20:23], v[204:207], v[44:47], v[20:23]
	v_mfma_f32_16x16x32_bf16 v[20:23], v[208:211], v[40:43], v[20:23]
	v_mfma_f32_16x16x32_bf16 v[20:23], v[212:215], v[24:27], v[20:23]
	ds_read_b128 v[200:203], v136 offset:24576
	ds_read_b128 v[204:207], v137 offset:24576
	ds_read_b128 v[208:211], v138 offset:24576
	ds_read_b128 v[212:215], v139 offset:24576
	s_waitcnt lgkmcnt(8)
	v_mfma_f32_16x16x32_bf16 v[16:19], v[216:219], v[48:51], 0
	v_mfma_f32_16x16x32_bf16 v[16:19], v[220:223], v[44:47], v[16:19]
	v_mfma_f32_16x16x32_bf16 v[16:19], v[224:227], v[40:43], v[16:19]
	v_mfma_f32_16x16x32_bf16 v[16:19], v[228:231], v[24:27], v[16:19]
	ds_read_b128 v[216:219], v140 offset:24576
	ds_read_b128 v[220:223], v141 offset:24576
	ds_read_b128 v[224:227], v142 offset:24576
	ds_read_b128 v[228:231], v143 offset:24576
	s_waitcnt lgkmcnt(8)
	v_mfma_f32_16x16x32_bf16 v[8:11], v[232:235], v[48:51], 0
	v_mfma_f32_16x16x32_bf16 v[8:11], v[236:239], v[44:47], v[8:11]
	v_mfma_f32_16x16x32_bf16 v[8:11], v[240:243], v[40:43], v[8:11]
	v_mfma_f32_16x16x32_bf16 v[8:11], v[244:247], v[24:27], v[8:11]
	ds_read_b128 v[232:235], v136 offset:32768
	ds_read_b128 v[236:239], v137 offset:32768
	ds_read_b128 v[240:243], v138 offset:32768
	ds_read_b128 v[244:247], v139 offset:32768
	s_waitcnt lgkmcnt(8)
	v_mfma_f32_16x16x32_bf16 v[4:7], v[200:203], v[48:51], 0
	v_mfma_f32_16x16x32_bf16 v[4:7], v[204:207], v[44:47], v[4:7]
	v_mfma_f32_16x16x32_bf16 v[4:7], v[208:211], v[40:43], v[4:7]
	v_mfma_f32_16x16x32_bf16 v[4:7], v[212:215], v[24:27], v[4:7]
	ds_read_b128 v[200:203], v140 offset:32768
	ds_read_b128 v[204:207], v141 offset:32768
	ds_read_b128 v[208:211], v142 offset:32768
	ds_read_b128 v[212:215], v143 offset:32768
	s_waitcnt lgkmcnt(8)
	v_mfma_f32_16x16x32_bf16 v[0:3], v[216:219], v[48:51], 0
	v_mfma_f32_16x16x32_bf16 v[0:3], v[220:223], v[44:47], v[0:3]
	v_mfma_f32_16x16x32_bf16 v[0:3], v[224:227], v[40:43], v[0:3]
	v_mfma_f32_16x16x32_bf16 v[0:3], v[228:231], v[24:27], v[0:3]
	s_waitcnt lgkmcnt(4)
	v_mfma_f32_16x16x32_bf16 v[12:15], v[232:235], v[48:51], 0
	v_mfma_f32_16x16x32_bf16 v[12:15], v[236:239], v[44:47], v[12:15]
	v_mfma_f32_16x16x32_bf16 v[12:15], v[240:243], v[40:43], v[12:15]
	v_mfma_f32_16x16x32_bf16 v[12:15], v[244:247], v[24:27], v[12:15]
	s_waitcnt lgkmcnt(0)
	s_barrier
	v_mfma_f32_16x16x32_bf16 v[216:219], v[200:203], v[48:51], 0
	v_mfma_f32_16x16x32_bf16 v[216:219], v[204:207], v[44:47], v[216:219]
	v_mfma_f32_16x16x32_bf16 v[216:219], v[208:211], v[40:43], v[216:219]
	v_mfma_f32_16x16x32_bf16 v[24:27], v[212:215], v[24:27], v[216:219]
	s_nop 2
	v_cndmask_b32_e64 v40, 0, 1, s[6:7]
	v_add_u32_e32 v149, s80, v71
	v_add_u32_e32 v148, s80, v78
	v_cmp_ne_u32_e64 s[4:5], 1, v40
	v_lshlrev_b32_e32 v50, 1, v60
	v_lshlrev_b32_e32 v48, 1, v62
	v_cmp_lt_i32_e64 s[10:11], -1, v151
	v_lshlrev_b32_e32 v46, 1, v64
	v_cmp_lt_i32_e64 s[8:9], -1, v150
	v_lshlrev_b32_e32 v44, 1, v66
	v_cmp_lt_i32_e64 s[6:7], -1, v149
	v_lshlrev_b32_e32 v42, 1, v68
	v_cmp_lt_i32_e64 s[2:3], -1, v148
	v_lshlrev_b32_e32 v40, 1, v70
	s_cbranch_vccnz .LBB0_703
	s_add_i32 s40, s36, -1
	v_min_i32_e32 v41, s40, v155
	v_cndmask_b32_e64 v156, 0, v41, s[18:19]
	v_readlane_b32 s29, v251, 45
	v_ashrrev_i32_e32 v157, 31, v156
	v_readlane_b32 s18, v251, 43
	s_mov_b32 m0, s29
	v_lshlrev_b64 v[156:157], s37, v[156:157]
	s_mov_b32 s29, s41
	v_readlane_b32 s19, v251, 44
	v_lshl_add_u64 v[156:157], v[156:157], 0, s[28:29]
	s_ashr_i32 s79, s78, 31
	v_mov_b64_e32 v[158:159], s[18:19]
	v_mad_u64_u32 v[160:161], s[18:19], v156, s30, v[158:159]
	v_mov_b32_e32 v156, v161
	v_mad_u64_u32 v[156:157], s[18:19], v157, s30, v[156:157]
	v_mov_b32_e32 v161, v156
	s_lshl_b64 s[18:19], s[78:79], 1
	v_lshl_add_u64 v[156:157], v[160:161], 0, s[18:19]
	v_lshl_add_u64 v[156:157], v[156:157], 0, v[56:57]
	v_min_i32_e32 v41, s40, v154
	global_load_lds_dwordx4 v[156:157], off
	v_cndmask_b32_e64 v156, 0, v41, s[16:17]
	v_ashrrev_i32_e32 v157, 31, v156
	v_lshlrev_b64 v[156:157], s37, v[156:157]
	v_lshl_add_u64 v[156:157], v[156:157], 0, s[28:29]
	v_mad_u64_u32 v[160:161], s[16:17], v156, s30, v[158:159]
	v_mov_b32_e32 v156, v161
	v_mad_u64_u32 v[156:157], s[16:17], v157, s30, v[156:157]
	v_mov_b32_e32 v161, v156
	v_lshl_add_u64 v[156:157], v[160:161], 0, s[18:19]
	v_mov_b32_e32 v77, v57
	v_readlane_b32 s16, v251, 47
	v_lshl_add_u64 v[156:157], v[156:157], 0, v[76:77]
	s_mov_b32 m0, s16
	v_min_i32_e32 v41, s40, v153
	global_load_lds_dwordx4 v[156:157], off
	v_cndmask_b32_e64 v156, 0, v41, s[14:15]
	v_ashrrev_i32_e32 v157, 31, v156
	v_lshlrev_b64 v[156:157], s37, v[156:157]
	v_lshl_add_u64 v[156:157], v[156:157], 0, s[28:29]
	v_mad_u64_u32 v[160:161], s[14:15], v156, s30, v[158:159]
	v_mov_b32_e32 v156, v161
	v_mad_u64_u32 v[156:157], s[14:15], v157, s30, v[156:157]
	v_mov_b32_e32 v161, v156
	v_lshl_add_u64 v[156:157], v[160:161], 0, s[18:19]
	v_mov_b32_e32 v51, v57
	v_readlane_b32 s14, v251, 49
	v_lshl_add_u64 v[156:157], v[156:157], 0, v[50:51]
	s_mov_b32 m0, s14
	v_min_i32_e32 v41, s40, v152
	global_load_lds_dwordx4 v[156:157], off
	v_cndmask_b32_e64 v156, 0, v41, s[12:13]
	v_ashrrev_i32_e32 v157, 31, v156
	v_lshlrev_b64 v[156:157], s37, v[156:157]
	v_lshl_add_u64 v[156:157], v[156:157], 0, s[28:29]
	v_mad_u64_u32 v[160:161], s[12:13], v156, s30, v[158:159]
	v_mov_b32_e32 v156, v161
	v_mad_u64_u32 v[156:157], s[12:13], v157, s30, v[156:157]
	v_mov_b32_e32 v161, v156
	v_lshl_add_u64 v[156:157], v[160:161], 0, s[18:19]
	v_mov_b32_e32 v49, v57
	v_readlane_b32 s12, v251, 51
	v_lshl_add_u64 v[156:157], v[156:157], 0, v[48:49]
	s_mov_b32 m0, s12
	v_min_i32_e32 v41, s40, v151
	global_load_lds_dwordx4 v[156:157], off
	v_cndmask_b32_e64 v156, 0, v41, s[10:11]
	v_ashrrev_i32_e32 v157, 31, v156
	v_lshlrev_b64 v[156:157], s37, v[156:157]
	v_lshl_add_u64 v[156:157], v[156:157], 0, s[28:29]
	v_mad_u64_u32 v[160:161], s[10:11], v156, s30, v[158:159]
	v_mov_b32_e32 v156, v161
	v_mad_u64_u32 v[156:157], s[10:11], v157, s30, v[156:157]
	v_mov_b32_e32 v161, v156
	v_lshl_add_u64 v[156:157], v[160:161], 0, s[18:19]
	v_mov_b32_e32 v47, v57
	v_readlane_b32 s10, v251, 53
	v_lshl_add_u64 v[156:157], v[156:157], 0, v[46:47]
	s_mov_b32 m0, s10
	v_min_i32_e32 v41, s40, v150
	global_load_lds_dwordx4 v[156:157], off
	v_cndmask_b32_e64 v156, 0, v41, s[8:9]
	v_ashrrev_i32_e32 v157, 31, v156
	v_lshlrev_b64 v[156:157], s37, v[156:157]
	v_lshl_add_u64 v[156:157], v[156:157], 0, s[28:29]
	v_mad_u64_u32 v[160:161], s[8:9], v156, s30, v[158:159]
	v_mov_b32_e32 v156, v161
	v_mad_u64_u32 v[156:157], s[8:9], v157, s30, v[156:157]
	v_mov_b32_e32 v161, v156
	v_lshl_add_u64 v[156:157], v[160:161], 0, s[18:19]
	v_mov_b32_e32 v45, v57
	v_readlane_b32 s8, v251, 55
	v_lshl_add_u64 v[156:157], v[156:157], 0, v[44:45]
	s_mov_b32 m0, s8
	v_min_i32_e32 v41, s40, v149
	global_load_lds_dwordx4 v[156:157], off
	v_cndmask_b32_e64 v156, 0, v41, s[6:7]
	v_ashrrev_i32_e32 v157, 31, v156
	v_lshlrev_b64 v[156:157], s37, v[156:157]
	v_lshl_add_u64 v[156:157], v[156:157], 0, s[28:29]
	v_mad_u64_u32 v[160:161], s[6:7], v156, s30, v[158:159]
	v_mov_b32_e32 v156, v161
	v_mad_u64_u32 v[156:157], s[6:7], v157, s30, v[156:157]
	v_mov_b32_e32 v161, v156
	v_lshl_add_u64 v[156:157], v[160:161], 0, s[18:19]
	v_mov_b32_e32 v43, v57
	v_readlane_b32 s6, v251, 57
	v_lshl_add_u64 v[156:157], v[156:157], 0, v[42:43]
	s_mov_b32 m0, s6
	v_min_i32_e32 v41, s40, v148
	global_load_lds_dwordx4 v[156:157], off
	v_cndmask_b32_e64 v156, 0, v41, s[2:3]
	v_ashrrev_i32_e32 v157, 31, v156
	v_lshlrev_b64 v[156:157], s37, v[156:157]
	v_lshl_add_u64 v[156:157], v[156:157], 0, s[28:29]
	v_mad_u64_u32 v[158:159], s[2:3], v156, s30, v[158:159]
	v_mov_b32_e32 v156, v159
	v_mad_u64_u32 v[156:157], s[2:3], v157, s30, v[156:157]
	v_mov_b32_e32 v159, v156
	v_lshl_add_u64 v[156:157], v[158:159], 0, s[18:19]
	v_mov_b32_e32 v41, v57
	v_readlane_b32 s2, v251, 59
	v_lshl_add_u64 v[156:157], v[156:157], 0, v[40:41]
	s_mov_b32 m0, s2
	s_nop 0
	global_load_lds_dwordx4 v[156:157], off

.LBB0_1188:
	v_readlane_b32 s64, v251, 21
	s_ashr_i32 s35, s34, 31
	v_readlane_b32 s74, v251, 31
	v_readlane_b32 s75, v251, 32
	v_readlane_b32 s78, v251, 35
	v_readlane_b32 s79, v251, 36
	s_lshl_b64 s[34:35], s[34:35], 14
	s_mov_b64 s[74:75], s[78:79]
	s_add_u32 s23, s74, s34
	s_addc_u32 s36, s75, s35
	s_lshl_b32 s28, s28, 7
	s_ashr_i32 s29, s28, 31
	s_lshl_b64 s[34:35], s[28:29], 2
	s_add_u32 s23, s23, s34
	s_addc_u32 s29, s36, s35
	s_add_u32 s34, s23, s55
	s_addc_u32 s35, s29, 0
	v_lshl_add_u64 v[226:227], v[220:221], 2, s[34:35]
	s_add_u32 s34, s6, 0x80
	s_addc_u32 s35, s7, 0
	s_add_u32 s23, s30, 0x100
	v_lshl_add_u64 v[228:229], v[226:227], 0, s[14:15]
	s_addc_u32 s29, s31, 0
	s_mov_b32 s63, -2
	v_readlane_b32 s65, v251, 22
	v_readlane_b32 s66, v251, 23
	v_readlane_b32 s67, v251, 24
	v_readlane_b32 s68, v251, 25
	v_readlane_b32 s69, v251, 26
	v_readlane_b32 s70, v251, 27
	v_readlane_b32 s71, v251, 28
	v_readlane_b32 s72, v251, 29
	v_readlane_b32 s73, v251, 30
	v_readlane_b32 s76, v251, 33
	v_readlane_b32 s77, v251, 34
	s_branch .Lpeel8_hdr

.Lpeel8_cont:
	s_waitcnt vmcnt(8)
	s_add_u32 s36, s34, 0x80
	s_waitcnt lgkmcnt(0)
	s_addc_u32 s37, s35, 0
	s_and_b64 s[30:31], s[30:31], exec
	v_mov_b32_e32 v217, v213
	v_mov_b32_e32 v219, v213
	s_cselect_b32 s37, s7, s37
	s_cselect_b32 s36, s6, s36
	s_cselect_b32 s31, s27, s29
	s_cselect_b32 s30, s26, s23
	s_barrier
	s_setprio 1
	s_waitcnt lgkmcnt(0)
	v_mfma_f32_16x16x128_f8f6f4 v[204:207], v[24:31], v[56:63], 0
	v_mfma_f32_16x16x128_f8f6f4 v[196:199], v[16:23], v[56:63], 0
	v_mfma_f32_16x16x128_f8f6f4 v[188:191], v[24:31], v[48:55], 0
	v_mfma_f32_16x16x128_f8f6f4 v[180:183], v[16:23], v[48:55], 0
	v_mfma_f32_16x16x128_f8f6f4 v[172:175], v[24:31], v[40:47], 0
	v_mfma_f32_16x16x128_f8f6f4 v[164:167], v[16:23], v[40:47], 0
	v_mfma_f32_16x16x128_f8f6f4 v[156:159], v[24:31], v[32:39], 0
	v_mfma_f32_16x16x128_f8f6f4 v[148:151], v[16:23], v[32:39], 0
	s_setprio 0
	s_setprio 1
	v_mfma_f32_16x16x128_f8f6f4 v[200:203], v[8:15], v[56:63], 0
	v_mfma_f32_16x16x128_f8f6f4 v[192:195], v[0:7], v[56:63], 0
	v_mfma_f32_16x16x128_f8f6f4 v[184:187], v[8:15], v[48:55], 0
	v_mfma_f32_16x16x128_f8f6f4 v[176:179], v[0:7], v[48:55], 0
	v_mfma_f32_16x16x128_f8f6f4 v[168:171], v[8:15], v[40:47], 0
	v_mfma_f32_16x16x128_f8f6f4 v[160:163], v[0:7], v[40:47], 0
	v_mfma_f32_16x16x128_f8f6f4 v[152:155], v[8:15], v[32:39], 0
	v_mfma_f32_16x16x128_f8f6f4 v[144:147], v[0:7], v[32:39], 0
	s_setprio 0
	s_barrier
	s_mov_b32 m0, s40
	v_lshl_add_u64 v[34:35], s[30:31], 0, v[208:209]
	s_add_u32 s64, s30, 0x40000
	ds_read_b128 v[40:43], v237 offset:16384
	ds_read_b128 v[44:47], v237 offset:17408
	ds_read_b128 v[48:51], v237 offset:18432
	ds_read_b128 v[52:55], v237 offset:19456
	ds_read_b128 v[56:59], v237 offset:20480
	ds_read_b128 v[60:63], v237 offset:21504
	ds_read_b128 v[240:243], v237 offset:22528
	ds_read_b128 v[244:247], v237 offset:23552
	global_load_lds_dwordx4 v[34:35], off
	v_lshl_add_u64 v[32:33], s[30:31], 0, v[210:211]
	s_mov_b32 m0, s41
	s_addc_u32 s65, s31, 0
	global_load_lds_dwordx4 v[32:33], off
	v_lshl_add_u64 v[36:37], s[64:65], 0, v[208:209]
	s_mov_b32 m0, s42
	v_mov_b32_e32 v215, v213
	global_load_lds_dwordx4 v[36:37], off
	v_lshl_add_u64 v[36:37], s[64:65], 0, v[210:211]
	s_mov_b32 m0, s43
	v_lshl_add_u64 v[38:39], s[36:37], 0, v[212:213]
	global_load_lds_dwordx4 v[36:37], off
	s_mov_b32 m0, s39
	v_lshl_add_u64 v[36:37], s[36:37], 0, v[214:215]
	global_load_lds_dwordx4 v212, s[36:37]
	s_mov_b32 m0, s44
	s_nop 0
	global_load_lds_dwordx4 v214, s[36:37]
	s_waitcnt vmcnt(8)
	s_waitcnt lgkmcnt(0)
	s_barrier
	s_setprio 1
	s_waitcnt lgkmcnt(0)
	v_mfma_f32_16x16x128_f8f6f4 v[140:143], v[24:31], v[40:47], 0
	v_mfma_f32_16x16x128_f8f6f4 v[132:135], v[16:23], v[40:47], 0
	v_mfma_f32_16x16x128_f8f6f4 v[124:127], v[24:31], v[48:55], 0
	v_mfma_f32_16x16x128_f8f6f4 v[116:119], v[16:23], v[48:55], 0
	v_mfma_f32_16x16x128_f8f6f4 v[108:111], v[24:31], v[56:63], 0
	v_mfma_f32_16x16x128_f8f6f4 v[100:103], v[16:23], v[56:63], 0
	v_mfma_f32_16x16x128_f8f6f4 v[92:95], v[24:31], v[240:247], 0
	v_mfma_f32_16x16x128_f8f6f4 v[84:87], v[16:23], v[240:247], 0
	s_setprio 0
	s_setprio 1
	v_mfma_f32_16x16x128_f8f6f4 v[136:139], v[8:15], v[40:47], 0
	v_mfma_f32_16x16x128_f8f6f4 v[128:131], v[0:7], v[40:47], 0
	v_mfma_f32_16x16x128_f8f6f4 v[120:123], v[8:15], v[48:55], 0
	v_mfma_f32_16x16x128_f8f6f4 v[112:115], v[0:7], v[48:55], 0
	v_mfma_f32_16x16x128_f8f6f4 v[104:107], v[8:15], v[56:63], 0
	v_mfma_f32_16x16x128_f8f6f4 v[96:99], v[0:7], v[56:63], 0
	v_mfma_f32_16x16x128_f8f6f4 v[88:91], v[8:15], v[240:247], 0
	v_mfma_f32_16x16x128_f8f6f4 v[80:83], v[0:7], v[240:247], 0
	s_setprio 0
	s_barrier
	s_branch .Lpeel8_sub3

.Lpeel8_sub3:
	s_add_i32 s64, 0, 0x18000
	s_add_i32 s65, 0, 0x1c000
	v_add_u32_e32 v12, s64, v236
	v_add_u32_e32 v28, s65, v236
	ds_read_b128 v[0:3], v12
	ds_read_b128 v[4:7], v12 offset:1024
	ds_read_b128 v[8:11], v12 offset:2048
	ds_read_b128 v[12:15], v12 offset:3072
	ds_read_b128 v[16:19], v28
	ds_read_b128 v[20:23], v28 offset:1024
	ds_read_b128 v[24:27], v28 offset:2048
	ds_read_b128 v[28:31], v28 offset:3072
	s_mov_b32 m0, s45
	v_lshl_add_u64 v[248:249], s[36:37], 0, v[216:217]
	ds_read_b128 v[40:43], v237 offset:32768
	ds_read_b128 v[44:47], v237 offset:33792
	ds_read_b128 v[48:51], v237 offset:34816
	ds_read_b128 v[52:55], v237 offset:35840
	ds_read_b128 v[56:59], v237 offset:36864
	ds_read_b128 v[60:63], v237 offset:37888
	ds_read_b128 v[240:243], v237 offset:38912
	ds_read_b128 v[244:247], v237 offset:39936
	global_load_lds_dwordx4 v[248:249], off
	v_lshl_add_u64 v[248:249], s[36:37], 0, v[218:219]
	s_mov_b32 m0, s46
	s_nop 0
	global_load_lds_dwordx4 v[248:249], off
	s_waitcnt vmcnt(8)
	s_waitcnt lgkmcnt(0)
	s_barrier
	s_setprio 1
	s_waitcnt lgkmcnt(0)
	v_mfma_f32_16x16x128_f8f6f4 v[204:207], v[0:7], v[40:47], v[204:207]
	v_mfma_f32_16x16x128_f8f6f4 v[196:199], v[8:15], v[40:47], v[196:199]
	v_mfma_f32_16x16x128_f8f6f4 v[188:191], v[0:7], v[48:55], v[188:191]
	v_mfma_f32_16x16x128_f8f6f4 v[180:183], v[8:15], v[48:55], v[180:183]
	v_mfma_f32_16x16x128_f8f6f4 v[172:175], v[0:7], v[56:63], v[172:175]
	v_mfma_f32_16x16x128_f8f6f4 v[164:167], v[8:15], v[56:63], v[164:167]
	v_mfma_f32_16x16x128_f8f6f4 v[156:159], v[0:7], v[240:247], v[156:159]
	v_mfma_f32_16x16x128_f8f6f4 v[148:151], v[8:15], v[240:247], v[148:151]
	s_setprio 0
	s_setprio 1
	v_mfma_f32_16x16x128_f8f6f4 v[200:203], v[16:23], v[40:47], v[200:203]
	v_mfma_f32_16x16x128_f8f6f4 v[192:195], v[24:31], v[40:47], v[192:195]
	v_mfma_f32_16x16x128_f8f6f4 v[184:187], v[16:23], v[48:55], v[184:187]
	v_mfma_f32_16x16x128_f8f6f4 v[176:179], v[24:31], v[48:55], v[176:179]
	v_mfma_f32_16x16x128_f8f6f4 v[168:171], v[16:23], v[56:63], v[168:171]
	v_mfma_f32_16x16x128_f8f6f4 v[160:163], v[24:31], v[56:63], v[160:163]
	v_mfma_f32_16x16x128_f8f6f4 v[152:155], v[16:23], v[240:247], v[152:155]
	v_mfma_f32_16x16x128_f8f6f4 v[144:147], v[24:31], v[240:247], v[144:147]
	s_setprio 0
	s_barrier
	s_add_i32 s36, s64, s38
	v_lshl_add_u64 v[34:35], v[34:35], 0, s[12:13]
	s_mov_b32 m0, s36
	ds_read_b128 v[40:43], v237 offset:49152
	ds_read_b128 v[44:47], v237 offset:50176
	ds_read_b128 v[48:51], v237 offset:51200
	ds_read_b128 v[52:55], v237 offset:52224
	ds_read_b128 v[56:59], v237 offset:53248
	ds_read_b128 v[60:63], v237 offset:54272
	ds_read_b128 v[240:243], v237 offset:55296
	ds_read_b128 v[244:247], v237 offset:56320
	global_load_lds_dwordx4 v[34:35], off
	s_add_i32 m0, s36, 0x2000
	s_add_u32 s30, s30, 0x40080
	v_lshl_add_u64 v[32:33], v[32:33], 0, s[12:13]
	s_addc_u32 s31, s31, 0
	s_add_i32 s36, s65, s38
	global_load_lds_dwordx4 v[32:33], off
	v_lshl_add_u64 v[32:33], s[30:31], 0, v[208:209]
	s_mov_b32 m0, s36
	s_nop 0
	global_load_lds_dwordx4 v[32:33], off
	v_lshl_add_u64 v[32:33], s[30:31], 0, v[210:211]
	s_add_i32 m0, s36, 0x2000
	s_nop 0
	global_load_lds_dwordx4 v[32:33], off
	v_lshl_add_u64 v[32:33], v[38:39], 0, s[12:13]
	s_mov_b32 m0, s50
	s_nop 0
	global_load_lds_dwordx4 v[32:33], off
	v_lshl_add_u64 v[32:33], v[36:37], 0, s[12:13]
	s_mov_b32 m0, s51
	s_nop 0
	global_load_lds_dwordx4 v[32:33], off
	s_waitcnt vmcnt(8)
	s_waitcnt lgkmcnt(0)
	s_barrier
	s_setprio 1
	s_waitcnt lgkmcnt(0)
	v_mfma_f32_16x16x128_f8f6f4 v[140:143], v[0:7], v[40:47], v[140:143]
	v_mfma_f32_16x16x128_f8f6f4 v[132:135], v[8:15], v[40:47], v[132:135]
	v_mfma_f32_16x16x128_f8f6f4 v[124:127], v[0:7], v[48:55], v[124:127]
	v_mfma_f32_16x16x128_f8f6f4 v[116:119], v[8:15], v[48:55], v[116:119]
	v_mfma_f32_16x16x128_f8f6f4 v[108:111], v[0:7], v[56:63], v[108:111]
	v_mfma_f32_16x16x128_f8f6f4 v[100:103], v[8:15], v[56:63], v[100:103]
	v_mfma_f32_16x16x128_f8f6f4 v[92:95], v[0:7], v[240:247], v[92:95]
	v_mfma_f32_16x16x128_f8f6f4 v[84:87], v[8:15], v[240:247], v[84:87]
	s_setprio 0
	s_setprio 1
	v_mfma_f32_16x16x128_f8f6f4 v[136:139], v[16:23], v[40:47], v[136:139]
	v_mfma_f32_16x16x128_f8f6f4 v[128:131], v[24:31], v[40:47], v[128:131]
	v_mfma_f32_16x16x128_f8f6f4 v[120:123], v[16:23], v[48:55], v[120:123]
	v_mfma_f32_16x16x128_f8f6f4 v[112:115], v[24:31], v[48:55], v[112:115]
	v_mfma_f32_16x16x128_f8f6f4 v[104:107], v[16:23], v[56:63], v[104:107]
	v_mfma_f32_16x16x128_f8f6f4 v[96:99], v[24:31], v[56:63], v[96:99]
	v_mfma_f32_16x16x128_f8f6f4 v[88:91], v[16:23], v[240:247], v[88:91]
	v_mfma_f32_16x16x128_f8f6f4 v[80:83], v[24:31], v[240:247], v[80:83]
	s_setprio 0
	s_barrier
	s_add_i32 s63, s63, 2
	s_add_u32 s34, s34, 0x100
	s_addc_u32 s35, s35, 0
	s_add_u32 s23, s23, 0x100
	s_addc_u32 s29, s29, 0
	s_cmp_gt_u32 s63, 13
	s_cbranch_scc1 .LBB0_1194
